# speedup vs baseline: 1.2578x; 1.2172x over previous
_Z11edge_kernelILi36ELb1EEvPKfS1_PKDF16_PKiS5_S1_S1_S1_S1_S1_PDF16_:
	s_load_dwordx8 s[4:11], s[0:1], 0x0
	s_load_dwordx8 s[12:19], s[0:1], 0x20
	s_load_dwordx4 s[20:23], s[0:1], 0x40
	s_load_dwordx2 s[24:25], s[0:1], 0x50
	v_readfirstlane_b32 s3, v0
	v_bfe_u32 v139, v0, 4, 2
	v_and_b32_e32 v140, 15, v0
	v_and_b32_e32 v142, 63, v0
	s_lshr_b32 s3, s3, 6
	s_lshl_b32 s2, s2, 1
	s_add_i32 s2, s2, s3
	v_lshlrev_b32_e32 v138, 8, v139
	v_lshl_or_b32 v138, v140, 4, v138
	v_lshlrev_b32_e32 v143, 4, v142
	v_lshl_or_b32 v141, v140, 2, v139
	v_lshlrev_b32_e32 v141, 2, v141
	v_mul_u32_u24_e32 v137, 0x900, v139
	v_lshl_or_b32 v137, v140, 4, v137
	v_mul_u32_u24_e32 v142, 36, v139
	s_mul_i32 s28, s2, 0x2400
	s_lshl_b32 s29, s2, 14
	s_lshl_b32 s30, s2, 2
	s_lshl_b32 s31, s2, 8
	s_lshl_b32 s33, s3, 10
	s_lshl_b32 s34, s3, 8
	s_addk_i32 s34, 0x4000
	s_waitcnt lgkmcnt(0)
	s_add_u32 s10, s10, s30
	s_addc_u32 s11, s11, 0
	s_add_u32 s12, s12, s30
	s_addc_u32 s13, s13, 0
	s_load_dword s35, s[10:11], 0x0
	s_load_dword s36, s[12:13], 0x0
	s_add_u32 s14, s14, s28
	s_addc_u32 s15, s15, 0
	global_load_dwordx4 v[0:3], v137, s[14:15] nt
	global_load_dwordx4 v[4:7], v137, s[14:15] offset:256 nt
	global_load_dwordx4 v[8:11], v137, s[14:15] offset:512 nt
	global_load_dwordx4 v[12:15], v137, s[14:15] offset:768 nt
	global_load_dwordx4 v[16:19], v137, s[14:15] offset:1024 nt
	global_load_dwordx4 v[20:23], v137, s[14:15] offset:1280 nt
	global_load_dwordx4 v[24:27], v137, s[14:15] offset:1536 nt
	global_load_dwordx4 v[28:31], v137, s[14:15] offset:1792 nt
	global_load_dwordx4 v[32:35], v137, s[14:15] offset:2048 nt
	s_add_u32 s22, s22, s33
	s_addc_u32 s23, s23, 0
	s_mov_b32 m0, s33
	s_add_u32 s18, s18, s29
	s_addc_u32 s19, s19, 0
	global_load_lds_dwordx4 v143, s[22:23]
	global_load_lds_dwordx4 v143, s[22:23] offset:2048
	s_add_u32 m0, m0, 0x1000
	s_add_u32 s22, s22, 0x1000
	s_addc_u32 s23, s23, 0
	global_load_lds_dwordx4 v143, s[22:23]
	global_load_lds_dwordx4 v143, s[22:23] offset:2048
	s_add_u32 m0, m0, 0x1000
	s_add_u32 s22, s22, 0x1000
	s_addc_u32 s23, s23, 0
	global_load_lds_dwordx4 v143, s[22:23]
	global_load_lds_dwordx4 v143, s[22:23] offset:2048
	s_add_u32 m0, m0, 0x1000
	s_add_u32 s22, s22, 0x1000
	s_addc_u32 s23, s23, 0
	global_load_lds_dwordx4 v143, s[22:23]
	global_load_lds_dwordx4 v143, s[22:23] offset:2048
	s_add_u32 s16, s16, s31
	s_addc_u32 s17, s17, 0
	s_add_u32 s20, s20, s31
	s_addc_u32 s21, s21, 0
	s_waitcnt lgkmcnt(0)
	s_lshl_b32 s36, s36, 7
	s_add_u32 s24, s24, s36
	s_addc_u32 s25, s25, 0
	s_lshl_b32 s37, s35, 7
	s_lshl_b32 s38, s35, 4
	s_add_u32 s4, s4, s37
	s_addc_u32 s5, s5, 0
	s_add_u32 s6, s6, s38
	s_addc_u32 s7, s7, 0
	v_mov_b32_e32 v157, 0
	v_mov_b32_e32 v156, v142
	v_lshl_add_u64 v[158:159], s[4:5], 0, v[156:157]
	v_lshl_add_u64 v[158:159], v[158:159], 0, 20
	v_cmp_eq_u32_e32 vcc, 3, v139
	s_nop 1
	v_mov_b32_e32 v154, s6
	v_mov_b32_e32 v155, s7
	v_cndmask_b32_e32 v158, v158, v154, vcc
	v_cndmask_b32_e32 v159, v159, v155, vcc
	global_load_dwordx4 v[144:147], v142, s[4:5] nt
	global_load_dword v148, v142, s[4:5] offset:16 nt
	global_load_dwordx4 v[150:153], v[158:159], off nt
	global_load_dword v136, v141, s[16:17] nt
	global_load_dword v128, v141, s[20:21] nt
	v_add_u32_e32 v142, s34, v141
	v_lshl_add_u32 v143, v139, 2, s34
	s_waitcnt vmcnt(2)
	s_barrier
	v_pk_mul_f32 v[160:161], v[144:145], v[0:1] op_sel_hi:[0,1]
	v_pk_mul_f32 v[162:163], v[144:145], v[2:3] op_sel_hi:[0,1]
	v_pk_mul_f32 v[164:165], v[144:145], v[4:5] op_sel:[1,0]
	v_pk_mul_f32 v[166:167], v[144:145], v[6:7] op_sel:[1,0]
	v_pk_fma_f32 v[160:161], v[146:147], v[8:9], v[160:161] op_sel_hi:[0,1,1]
	v_pk_fma_f32 v[162:163], v[146:147], v[10:11], v[162:163] op_sel_hi:[0,1,1]
	v_pk_fma_f32 v[164:165], v[146:147], v[12:13], v[164:165] op_sel:[1,0,0]
	v_pk_fma_f32 v[166:167], v[146:147], v[14:15], v[166:167] op_sel:[1,0,0]
	v_pk_fma_f32 v[160:161], v[148:149], v[16:17], v[160:161] op_sel_hi:[0,1,1]
	v_pk_fma_f32 v[162:163], v[148:149], v[18:19], v[162:163] op_sel_hi:[0,1,1]
	v_pk_fma_f32 v[164:165], v[150:151], v[20:21], v[164:165] op_sel_hi:[0,1,1]
	v_pk_fma_f32 v[166:167], v[150:151], v[22:23], v[166:167] op_sel_hi:[0,1,1]
	v_pk_fma_f32 v[160:161], v[150:151], v[24:25], v[160:161] op_sel:[1,0,0]
	v_pk_fma_f32 v[162:163], v[150:151], v[26:27], v[162:163] op_sel:[1,0,0]
	v_pk_fma_f32 v[164:165], v[152:153], v[28:29], v[164:165] op_sel_hi:[0,1,1]
	v_pk_fma_f32 v[166:167], v[152:153], v[30:31], v[166:167] op_sel_hi:[0,1,1]
	v_pk_fma_f32 v[160:161], v[152:153], v[32:33], v[160:161] op_sel:[1,0,0]
	v_pk_fma_f32 v[162:163], v[152:153], v[34:35], v[162:163] op_sel:[1,0,0]
	v_pk_add_f32 v[160:161], v[160:161], v[164:165]
	v_pk_add_f32 v[162:163], v[162:163], v[166:167]
	s_nop 1
	v_permlane16_swap_b32_e32 v160, v161
	v_permlane16_swap_b32_e32 v162, v163
	v_add_f32_e32 v160, v160, v161
	v_add_f32_e32 v162, v162, v163
	s_nop 1
	v_permlane32_swap_b32_e32 v160, v162
	v_add_f32_e32 v160, v160, v162
	s_waitcnt vmcnt(1)
	v_add_f32_e32 v160, v160, v136
	v_max_f32_e32 v160, 0, v160
	ds_write_b32 v142, v160
	ds_read2_b32 v[144:145], v143 offset0:0 offset1:4
	ds_read2_b32 v[146:147], v143 offset0:8 offset1:12
	ds_read2_b32 v[148:149], v143 offset0:16 offset1:20
	ds_read2_b32 v[150:151], v143 offset0:24 offset1:28
	ds_read2_b32 v[152:153], v143 offset0:32 offset1:36
	ds_read2_b32 v[154:155], v143 offset0:40 offset1:44
	ds_read2_b32 v[156:157], v143 offset0:48 offset1:52
	ds_read2_b32 v[158:159], v143 offset0:56 offset1:60
	ds_read_b128 v[0:3], v138
	ds_read_b128 v[4:7], v138 offset:1024
	ds_read_b128 v[8:11], v138 offset:2048
	ds_read_b128 v[12:15], v138 offset:3072
	ds_read_b128 v[16:19], v138 offset:4096
	ds_read_b128 v[20:23], v138 offset:5120
	s_waitcnt lgkmcnt(6)
	v_cmp_neq_f32_e64 s[40:41], 0, v144
	v_cmp_neq_f32_e64 s[42:43], 0, v145
	v_cmp_neq_f32_e64 s[44:45], 0, v146
	v_cmp_neq_f32_e64 s[46:47], 0, v147
	v_cmp_neq_f32_e64 s[48:49], 0, v148
	v_cmp_neq_f32_e64 s[50:51], 0, v149
	v_cmp_neq_f32_e64 s[52:53], 0, v150
	v_cmp_neq_f32_e64 s[54:55], 0, v151
	v_cmp_neq_f32_e64 s[56:57], 0, v152
	v_cmp_neq_f32_e64 s[58:59], 0, v153
	v_cmp_neq_f32_e64 s[60:61], 0, v154
	v_cmp_neq_f32_e64 s[62:63], 0, v155
	v_cmp_neq_f32_e64 s[64:65], 0, v156
	v_cmp_neq_f32_e64 s[66:67], 0, v157
	v_cmp_neq_f32_e64 s[68:69], 0, v158
	v_cmp_neq_f32_e64 s[70:71], 0, v159
	s_mov_b64 exec, s[40:41]
	global_load_dwordx4 v[64:67], v138, s[18:19] nt
	s_mov_b64 exec, s[42:43]
	global_load_dwordx4 v[68:71], v138, s[18:19] offset:1024 nt
	s_mov_b64 exec, s[44:45]
	global_load_dwordx4 v[72:75], v138, s[18:19] offset:2048 nt
	s_mov_b64 exec, s[46:47]
	global_load_dwordx4 v[76:79], v138, s[18:19] offset:3072 nt
	s_add_u32 s18, s18, 0x1000
	s_addc_u32 s19, s19, 0
	s_mov_b64 exec, s[48:49]
	global_load_dwordx4 v[80:83], v138, s[18:19] nt
	s_mov_b64 exec, s[50:51]
	global_load_dwordx4 v[84:87], v138, s[18:19] offset:1024 nt
	s_mov_b64 exec, s[52:53]
	global_load_dwordx4 v[88:91], v138, s[18:19] offset:2048 nt
	s_mov_b64 exec, s[54:55]
	global_load_dwordx4 v[92:95], v138, s[18:19] offset:3072 nt
	s_add_u32 s18, s18, 0x1000
	s_addc_u32 s19, s19, 0
	s_mov_b64 exec, s[56:57]
	global_load_dwordx4 v[96:99], v138, s[18:19] nt
	s_mov_b64 exec, s[58:59]
	global_load_dwordx4 v[100:103], v138, s[18:19] offset:1024 nt
	s_mov_b64 exec, s[60:61]
	global_load_dwordx4 v[104:107], v138, s[18:19] offset:2048 nt
	s_mov_b64 exec, s[62:63]
	global_load_dwordx4 v[108:111], v138, s[18:19] offset:3072 nt
	s_add_u32 s18, s18, 0x1000
	s_addc_u32 s19, s19, 0
	s_mov_b64 exec, s[64:65]
	global_load_dwordx4 v[112:115], v138, s[18:19] nt
	s_mov_b64 exec, s[66:67]
	global_load_dwordx4 v[116:119], v138, s[18:19] offset:1024 nt
	s_mov_b64 exec, s[68:69]
	global_load_dwordx4 v[120:123], v138, s[18:19] offset:2048 nt
	s_mov_b64 exec, s[70:71]
	global_load_dwordx4 v[124:127], v138, s[18:19] offset:3072 nt
	s_mov_b64 exec, -1
	v_mov_b32_e32 v160, 0
	v_mov_b32_e32 v161, 0
	v_mov_b32_e32 v162, 0
	v_mov_b32_e32 v163, 0
	v_mov_b32_e32 v164, 0
	v_mov_b32_e32 v165, 0
	v_mov_b32_e32 v166, 0
	v_mov_b32_e32 v167, 0
	s_waitcnt lgkmcnt(0)
	ds_read_b128 v[24:27], v138 offset:6144
	ds_read_b128 v[28:31], v138 offset:7168
	ds_read_b128 v[32:35], v138 offset:8192
	ds_read_b128 v[36:39], v138 offset:9216
	ds_read_b128 v[40:43], v138 offset:10240
	ds_read_b128 v[44:47], v138 offset:11264
	ds_read_b128 v[48:51], v138 offset:12288
	ds_read_b128 v[52:55], v138 offset:13312
	ds_read_b128 v[56:59], v138 offset:14336
	ds_read_b128 v[60:63], v138 offset:15360
	s_waitcnt vmcnt(0)
	s_mov_b64 exec, s[40:41]
	v_pk_fma_f32 v[160:161], v[144:145], v[64:65], v[160:161] op_sel_hi:[0,1,1]
	v_pk_fma_f32 v[162:163], v[144:145], v[66:67], v[162:163] op_sel_hi:[0,1,1]
	s_mov_b64 exec, s[42:43]
	v_pk_fma_f32 v[164:165], v[144:145], v[68:69], v[164:165] op_sel:[1,0,0]
	v_pk_fma_f32 v[166:167], v[144:145], v[70:71], v[166:167] op_sel:[1,0,0]
	s_mov_b64 exec, s[44:45]
	v_pk_fma_f32 v[160:161], v[146:147], v[72:73], v[160:161] op_sel_hi:[0,1,1]
	v_pk_fma_f32 v[162:163], v[146:147], v[74:75], v[162:163] op_sel_hi:[0,1,1]
	s_mov_b64 exec, s[46:47]
	v_pk_fma_f32 v[164:165], v[146:147], v[76:77], v[164:165] op_sel:[1,0,0]
	v_pk_fma_f32 v[166:167], v[146:147], v[78:79], v[166:167] op_sel:[1,0,0]
	s_mov_b64 exec, s[48:49]
	v_pk_fma_f32 v[160:161], v[148:149], v[80:81], v[160:161] op_sel_hi:[0,1,1]
	v_pk_fma_f32 v[162:163], v[148:149], v[82:83], v[162:163] op_sel_hi:[0,1,1]
	s_mov_b64 exec, s[50:51]
	v_pk_fma_f32 v[164:165], v[148:149], v[84:85], v[164:165] op_sel:[1,0,0]
	v_pk_fma_f32 v[166:167], v[148:149], v[86:87], v[166:167] op_sel:[1,0,0]
	s_mov_b64 exec, s[52:53]
	v_pk_fma_f32 v[160:161], v[150:151], v[88:89], v[160:161] op_sel_hi:[0,1,1]
	v_pk_fma_f32 v[162:163], v[150:151], v[90:91], v[162:163] op_sel_hi:[0,1,1]
	s_mov_b64 exec, s[54:55]
	v_pk_fma_f32 v[164:165], v[150:151], v[92:93], v[164:165] op_sel:[1,0,0]
	v_pk_fma_f32 v[166:167], v[150:151], v[94:95], v[166:167] op_sel:[1,0,0]
	s_mov_b64 exec, s[56:57]
	v_pk_fma_f32 v[160:161], v[152:153], v[96:97], v[160:161] op_sel_hi:[0,1,1]
	v_pk_fma_f32 v[162:163], v[152:153], v[98:99], v[162:163] op_sel_hi:[0,1,1]
	s_mov_b64 exec, s[58:59]
	v_pk_fma_f32 v[164:165], v[152:153], v[100:101], v[164:165] op_sel:[1,0,0]
	v_pk_fma_f32 v[166:167], v[152:153], v[102:103], v[166:167] op_sel:[1,0,0]
	s_mov_b64 exec, s[60:61]
	v_pk_fma_f32 v[160:161], v[154:155], v[104:105], v[160:161] op_sel_hi:[0,1,1]
	v_pk_fma_f32 v[162:163], v[154:155], v[106:107], v[162:163] op_sel_hi:[0,1,1]
	s_mov_b64 exec, s[62:63]
	v_pk_fma_f32 v[164:165], v[154:155], v[108:109], v[164:165] op_sel:[1,0,0]
	v_pk_fma_f32 v[166:167], v[154:155], v[110:111], v[166:167] op_sel:[1,0,0]
	s_mov_b64 exec, s[64:65]
	v_pk_fma_f32 v[160:161], v[156:157], v[112:113], v[160:161] op_sel_hi:[0,1,1]
	v_pk_fma_f32 v[162:163], v[156:157], v[114:115], v[162:163] op_sel_hi:[0,1,1]
	s_mov_b64 exec, s[66:67]
	v_pk_fma_f32 v[164:165], v[156:157], v[116:117], v[164:165] op_sel:[1,0,0]
	v_pk_fma_f32 v[166:167], v[156:157], v[118:119], v[166:167] op_sel:[1,0,0]
	s_mov_b64 exec, s[68:69]
	v_pk_fma_f32 v[160:161], v[158:159], v[120:121], v[160:161] op_sel_hi:[0,1,1]
	v_pk_fma_f32 v[162:163], v[158:159], v[122:123], v[162:163] op_sel_hi:[0,1,1]
	s_mov_b64 exec, s[70:71]
	v_pk_fma_f32 v[164:165], v[158:159], v[124:125], v[164:165] op_sel:[1,0,0]
	v_pk_fma_f32 v[166:167], v[158:159], v[126:127], v[166:167] op_sel:[1,0,0]
	s_mov_b64 exec, -1
	v_pk_add_f32 v[160:161], v[160:161], v[164:165]
	v_pk_add_f32 v[162:163], v[162:163], v[166:167]
	s_nop 1
	v_permlane16_swap_b32_e32 v160, v161
	v_permlane16_swap_b32_e32 v162, v163
	v_add_f32_e32 v160, v160, v161
	v_add_f32_e32 v162, v162, v163
	s_nop 1
	v_permlane32_swap_b32_e32 v160, v162
	v_add_f32_e32 v160, v160, v162
	v_add_f32_e32 v160, v160, v128
	s_waitcnt lgkmcnt(0)
	ds_write_b32 v142, v160
	ds_read2_b32 v[144:145], v143 offset0:0 offset1:4
	ds_read2_b32 v[146:147], v143 offset0:8 offset1:12
	ds_read2_b32 v[148:149], v143 offset0:16 offset1:20
	ds_read2_b32 v[150:151], v143 offset0:24 offset1:28
	ds_read2_b32 v[152:153], v143 offset0:32 offset1:36
	ds_read2_b32 v[154:155], v143 offset0:40 offset1:44
	ds_read2_b32 v[156:157], v143 offset0:48 offset1:52
	ds_read2_b32 v[158:159], v143 offset0:56 offset1:60
	v_lshlrev_b32_e32 v136, 3, v140
	v_lshl_or_b32 v136, v139, 2, v136
	v_cmp_gt_u32_e32 vcc, 2, v139
	s_waitcnt lgkmcnt(0)
	v_pk_mul_f32 v[160:161], v[144:145], v[0:1] op_sel_hi:[0,1]
	v_pk_mul_f32 v[162:163], v[144:145], v[2:3] op_sel_hi:[0,1]
	v_pk_mul_f32 v[164:165], v[144:145], v[4:5] op_sel:[1,0]
	v_pk_mul_f32 v[166:167], v[144:145], v[6:7] op_sel:[1,0]
	v_pk_fma_f32 v[160:161], v[146:147], v[8:9], v[160:161] op_sel_hi:[0,1,1]
	v_pk_fma_f32 v[162:163], v[146:147], v[10:11], v[162:163] op_sel_hi:[0,1,1]
	v_pk_fma_f32 v[164:165], v[146:147], v[12:13], v[164:165] op_sel:[1,0,0]
	v_pk_fma_f32 v[166:167], v[146:147], v[14:15], v[166:167] op_sel:[1,0,0]
	v_pk_fma_f32 v[160:161], v[148:149], v[16:17], v[160:161] op_sel_hi:[0,1,1]
	v_pk_fma_f32 v[162:163], v[148:149], v[18:19], v[162:163] op_sel_hi:[0,1,1]
	v_pk_fma_f32 v[164:165], v[148:149], v[20:21], v[164:165] op_sel:[1,0,0]
	v_pk_fma_f32 v[166:167], v[148:149], v[22:23], v[166:167] op_sel:[1,0,0]
	v_pk_fma_f32 v[160:161], v[150:151], v[24:25], v[160:161] op_sel_hi:[0,1,1]
	v_pk_fma_f32 v[162:163], v[150:151], v[26:27], v[162:163] op_sel_hi:[0,1,1]
	v_pk_fma_f32 v[164:165], v[150:151], v[28:29], v[164:165] op_sel:[1,0,0]
	v_pk_fma_f32 v[166:167], v[150:151], v[30:31], v[166:167] op_sel:[1,0,0]
	v_pk_fma_f32 v[160:161], v[152:153], v[32:33], v[160:161] op_sel_hi:[0,1,1]
	v_pk_fma_f32 v[162:163], v[152:153], v[34:35], v[162:163] op_sel_hi:[0,1,1]
	v_pk_fma_f32 v[164:165], v[152:153], v[36:37], v[164:165] op_sel:[1,0,0]
	v_pk_fma_f32 v[166:167], v[152:153], v[38:39], v[166:167] op_sel:[1,0,0]
	v_pk_fma_f32 v[160:161], v[154:155], v[40:41], v[160:161] op_sel_hi:[0,1,1]
	v_pk_fma_f32 v[162:163], v[154:155], v[42:43], v[162:163] op_sel_hi:[0,1,1]
	v_pk_fma_f32 v[164:165], v[154:155], v[44:45], v[164:165] op_sel:[1,0,0]
	v_pk_fma_f32 v[166:167], v[154:155], v[46:47], v[166:167] op_sel:[1,0,0]
	v_pk_fma_f32 v[160:161], v[156:157], v[48:49], v[160:161] op_sel_hi:[0,1,1]
	v_pk_fma_f32 v[162:163], v[156:157], v[50:51], v[162:163] op_sel_hi:[0,1,1]
	v_pk_fma_f32 v[164:165], v[156:157], v[52:53], v[164:165] op_sel:[1,0,0]
	v_pk_fma_f32 v[166:167], v[156:157], v[54:55], v[166:167] op_sel:[1,0,0]
	v_pk_fma_f32 v[160:161], v[158:159], v[56:57], v[160:161] op_sel_hi:[0,1,1]
	v_pk_fma_f32 v[162:163], v[158:159], v[58:59], v[162:163] op_sel_hi:[0,1,1]
	v_pk_fma_f32 v[164:165], v[158:159], v[60:61], v[164:165] op_sel:[1,0,0]
	v_pk_fma_f32 v[166:167], v[158:159], v[62:63], v[166:167] op_sel:[1,0,0]
	v_pk_add_f32 v[160:161], v[160:161], v[164:165]
	v_pk_add_f32 v[162:163], v[162:163], v[166:167]
	s_nop 1
	v_permlane16_swap_b32_e32 v160, v162
	v_permlane16_swap_b32_e32 v161, v163
	v_add_f32_e32 v160, v160, v162
	v_add_f32_e32 v161, v161, v163
	v_mov_b32_e32 v144, v160
	v_mov_b32_e32 v145, v161
	s_nop 1
	v_permlane32_swap_b32_e32 v160, v144
	v_permlane32_swap_b32_e32 v161, v145
	v_add_f32_e32 v160, v160, v144
	v_add_f32_e32 v161, v161, v145
	v_cvt_pk_f16_f32 v137, v160, v161
	s_and_saveexec_b64 s[4:5], vcc
	global_atomic_pk_add_f16 v136, v137, s[24:25]
	s_endpgm
	.p2align	8

_Z11edge_kernelILi64ELb0EEvPKfS1_PKDF16_PKiS5_S1_S1_S1_S1_S1_PDF16_:
	s_load_dwordx16 s[4:19], s[0:1], 0x10
	s_load_dwordx2 s[20:21], s[0:1], 0x50
	v_readfirstlane_b32 s3, v0
	v_bfe_u32 v139, v0, 4, 2
	v_and_b32_e32 v140, 15, v0
	v_and_b32_e32 v142, 63, v0
	s_lshr_b32 s3, s3, 6
	s_lshl_b32 s2, s2, 1
	s_add_i32 s2, s2, s3
	v_lshlrev_b32_e32 v138, 8, v139
	v_lshl_or_b32 v138, v140, 4, v138
	v_lshlrev_b32_e32 v143, 4, v142
	v_lshl_or_b32 v141, v140, 2, v139
	v_lshlrev_b32_e32 v141, 2, v141
	v_lshlrev_b32_e32 v142, 5, v139
	v_lshlrev_b32_e32 v137, 12, v139
	v_lshl_or_b32 v137, v140, 4, v137
	s_lshl_b32 s28, s2, 14
	s_lshl_b32 s29, s2, 14
	s_lshl_b32 s30, s2, 2
	s_lshl_b32 s31, s2, 8
	s_lshl_b32 s33, s3, 10
	s_lshl_b32 s34, s3, 8
	s_addk_i32 s34, 0x4000
	s_waitcnt lgkmcnt(0)
	s_add_u32 s6, s6, s30
	s_addc_u32 s7, s7, 0
	s_add_u32 s8, s8, s30
	s_addc_u32 s9, s9, 0
	s_load_dword s35, s[6:7], 0x0
	s_load_dword s36, s[8:9], 0x0
	s_add_u32 s10, s10, s28
	s_addc_u32 s11, s11, 0
	global_load_dwordx4 v[0:3], v137, s[10:11] nt
	global_load_dwordx4 v[4:7], v137, s[10:11] offset:256 nt
	global_load_dwordx4 v[8:11], v137, s[10:11] offset:512 nt
	global_load_dwordx4 v[12:15], v137, s[10:11] offset:768 nt
	global_load_dwordx4 v[16:19], v137, s[10:11] offset:1024 nt
	global_load_dwordx4 v[20:23], v137, s[10:11] offset:1280 nt
	global_load_dwordx4 v[24:27], v137, s[10:11] offset:1536 nt
	global_load_dwordx4 v[28:31], v137, s[10:11] offset:1792 nt
	global_load_dwordx4 v[32:35], v137, s[10:11] offset:2048 nt
	global_load_dwordx4 v[36:39], v137, s[10:11] offset:2304 nt
	global_load_dwordx4 v[40:43], v137, s[10:11] offset:2560 nt
	global_load_dwordx4 v[44:47], v137, s[10:11] offset:2816 nt
	global_load_dwordx4 v[48:51], v137, s[10:11] offset:3072 nt
	global_load_dwordx4 v[52:55], v137, s[10:11] offset:3328 nt
	global_load_dwordx4 v[56:59], v137, s[10:11] offset:3584 nt
	global_load_dwordx4 v[60:63], v137, s[10:11] offset:3840 nt
	s_add_u32 s18, s18, s33
	s_addc_u32 s19, s19, 0
	s_mov_b32 m0, s33
	s_add_u32 s14, s14, s29
	s_addc_u32 s15, s15, 0
	global_load_lds_dwordx4 v143, s[18:19]
	global_load_lds_dwordx4 v143, s[18:19] offset:2048
	s_add_u32 m0, m0, 0x1000
	s_add_u32 s18, s18, 0x1000
	s_addc_u32 s19, s19, 0
	global_load_lds_dwordx4 v143, s[18:19]
	global_load_lds_dwordx4 v143, s[18:19] offset:2048
	s_add_u32 m0, m0, 0x1000
	s_add_u32 s18, s18, 0x1000
	s_addc_u32 s19, s19, 0
	global_load_lds_dwordx4 v143, s[18:19]
	global_load_lds_dwordx4 v143, s[18:19] offset:2048
	s_add_u32 m0, m0, 0x1000
	s_add_u32 s18, s18, 0x1000
	s_addc_u32 s19, s19, 0
	global_load_lds_dwordx4 v143, s[18:19]
	global_load_lds_dwordx4 v143, s[18:19] offset:2048
	s_add_u32 s12, s12, s31
	s_addc_u32 s13, s13, 0
	s_add_u32 s16, s16, s31
	s_addc_u32 s17, s17, 0
	s_waitcnt lgkmcnt(0)
	s_lshl_b32 s36, s36, 7
	s_add_u32 s20, s20, s36
	s_addc_u32 s21, s21, 0
	s_lshl_b32 s37, s35, 7
	s_add_u32 s4, s4, s37
	s_addc_u32 s5, s5, 0
	global_load_dwordx4 v[128:131], v142, s[4:5] nt
	global_load_dwordx4 v[132:135], v142, s[4:5] offset:16 nt
	global_load_dword v136, v141, s[12:13] nt
	global_load_dword v137, v141, s[16:17] nt
	v_add_u32_e32 v142, s34, v141
	v_lshl_add_u32 v143, v139, 2, s34
	s_waitcnt vmcnt(2)
	s_barrier
	v_cvt_f32_f16_e32 v144, v128
	v_cvt_f32_f16_sdwa v145, v128 dst_sel:DWORD dst_unused:UNUSED_PAD src0_sel:WORD_1
	v_cvt_f32_f16_e32 v146, v129
	v_cvt_f32_f16_sdwa v147, v129 dst_sel:DWORD dst_unused:UNUSED_PAD src0_sel:WORD_1
	v_cvt_f32_f16_e32 v148, v130
	v_cvt_f32_f16_sdwa v149, v130 dst_sel:DWORD dst_unused:UNUSED_PAD src0_sel:WORD_1
	v_cvt_f32_f16_e32 v150, v131
	v_cvt_f32_f16_sdwa v151, v131 dst_sel:DWORD dst_unused:UNUSED_PAD src0_sel:WORD_1
	v_cvt_f32_f16_e32 v152, v132
	v_cvt_f32_f16_sdwa v153, v132 dst_sel:DWORD dst_unused:UNUSED_PAD src0_sel:WORD_1
	v_cvt_f32_f16_e32 v154, v133
	v_cvt_f32_f16_sdwa v155, v133 dst_sel:DWORD dst_unused:UNUSED_PAD src0_sel:WORD_1
	v_cvt_f32_f16_e32 v156, v134
	v_cvt_f32_f16_sdwa v157, v134 dst_sel:DWORD dst_unused:UNUSED_PAD src0_sel:WORD_1
	v_cvt_f32_f16_e32 v158, v135
	v_cvt_f32_f16_sdwa v159, v135 dst_sel:DWORD dst_unused:UNUSED_PAD src0_sel:WORD_1
	v_max_f32_e32 v144, 0, v144
	v_max_f32_e32 v145, 0, v145
	v_max_f32_e32 v146, 0, v146
	v_max_f32_e32 v147, 0, v147
	v_max_f32_e32 v148, 0, v148
	v_max_f32_e32 v149, 0, v149
	v_max_f32_e32 v150, 0, v150
	v_max_f32_e32 v151, 0, v151
	v_max_f32_e32 v152, 0, v152
	v_max_f32_e32 v153, 0, v153
	v_max_f32_e32 v154, 0, v154
	v_max_f32_e32 v155, 0, v155
	v_max_f32_e32 v156, 0, v156
	v_max_f32_e32 v157, 0, v157
	v_max_f32_e32 v158, 0, v158
	v_max_f32_e32 v159, 0, v159
	v_pk_mul_f32 v[160:161], v[144:145], v[0:1] op_sel_hi:[0,1]
	v_pk_mul_f32 v[162:163], v[144:145], v[2:3] op_sel_hi:[0,1]
	v_pk_mul_f32 v[164:165], v[144:145], v[4:5] op_sel:[1,0]
	v_pk_mul_f32 v[166:167], v[144:145], v[6:7] op_sel:[1,0]
	v_pk_fma_f32 v[160:161], v[146:147], v[8:9], v[160:161] op_sel_hi:[0,1,1]
	v_pk_fma_f32 v[162:163], v[146:147], v[10:11], v[162:163] op_sel_hi:[0,1,1]
	v_pk_fma_f32 v[164:165], v[146:147], v[12:13], v[164:165] op_sel:[1,0,0]
	v_pk_fma_f32 v[166:167], v[146:147], v[14:15], v[166:167] op_sel:[1,0,0]
	v_pk_fma_f32 v[160:161], v[148:149], v[16:17], v[160:161] op_sel_hi:[0,1,1]
	v_pk_fma_f32 v[162:163], v[148:149], v[18:19], v[162:163] op_sel_hi:[0,1,1]
	v_pk_fma_f32 v[164:165], v[148:149], v[20:21], v[164:165] op_sel:[1,0,0]
	v_pk_fma_f32 v[166:167], v[148:149], v[22:23], v[166:167] op_sel:[1,0,0]
	v_pk_fma_f32 v[160:161], v[150:151], v[24:25], v[160:161] op_sel_hi:[0,1,1]
	v_pk_fma_f32 v[162:163], v[150:151], v[26:27], v[162:163] op_sel_hi:[0,1,1]
	v_pk_fma_f32 v[164:165], v[150:151], v[28:29], v[164:165] op_sel:[1,0,0]
	v_pk_fma_f32 v[166:167], v[150:151], v[30:31], v[166:167] op_sel:[1,0,0]
	v_pk_fma_f32 v[160:161], v[152:153], v[32:33], v[160:161] op_sel_hi:[0,1,1]
	v_pk_fma_f32 v[162:163], v[152:153], v[34:35], v[162:163] op_sel_hi:[0,1,1]
	v_pk_fma_f32 v[164:165], v[152:153], v[36:37], v[164:165] op_sel:[1,0,0]
	v_pk_fma_f32 v[166:167], v[152:153], v[38:39], v[166:167] op_sel:[1,0,0]
	v_pk_fma_f32 v[160:161], v[154:155], v[40:41], v[160:161] op_sel_hi:[0,1,1]
	v_pk_fma_f32 v[162:163], v[154:155], v[42:43], v[162:163] op_sel_hi:[0,1,1]
	v_pk_fma_f32 v[164:165], v[154:155], v[44:45], v[164:165] op_sel:[1,0,0]
	v_pk_fma_f32 v[166:167], v[154:155], v[46:47], v[166:167] op_sel:[1,0,0]
	v_pk_fma_f32 v[160:161], v[156:157], v[48:49], v[160:161] op_sel_hi:[0,1,1]
	v_pk_fma_f32 v[162:163], v[156:157], v[50:51], v[162:163] op_sel_hi:[0,1,1]
	v_pk_fma_f32 v[164:165], v[156:157], v[52:53], v[164:165] op_sel:[1,0,0]
	v_pk_fma_f32 v[166:167], v[156:157], v[54:55], v[166:167] op_sel:[1,0,0]
	v_pk_fma_f32 v[160:161], v[158:159], v[56:57], v[160:161] op_sel_hi:[0,1,1]
	v_pk_fma_f32 v[162:163], v[158:159], v[58:59], v[162:163] op_sel_hi:[0,1,1]
	v_pk_fma_f32 v[164:165], v[158:159], v[60:61], v[164:165] op_sel:[1,0,0]
	v_pk_fma_f32 v[166:167], v[158:159], v[62:63], v[166:167] op_sel:[1,0,0]
	v_pk_add_f32 v[160:161], v[160:161], v[164:165]
	v_pk_add_f32 v[162:163], v[162:163], v[166:167]
	s_nop 1
	v_permlane16_swap_b32_e32 v160, v161
	v_permlane16_swap_b32_e32 v162, v163
	v_add_f32_e32 v160, v160, v161
	v_add_f32_e32 v162, v162, v163
	s_nop 1
	v_permlane32_swap_b32_e32 v160, v162
	v_add_f32_e32 v160, v160, v162
	s_waitcnt vmcnt(1)
	v_add_f32_e32 v160, v160, v136
	v_max_f32_e32 v160, 0, v160
	ds_write_b32 v142, v160
	ds_read2_b32 v[144:145], v143 offset0:0 offset1:4
	ds_read2_b32 v[146:147], v143 offset0:8 offset1:12
	ds_read2_b32 v[148:149], v143 offset0:16 offset1:20
	ds_read2_b32 v[150:151], v143 offset0:24 offset1:28
	ds_read2_b32 v[152:153], v143 offset0:32 offset1:36
	ds_read2_b32 v[154:155], v143 offset0:40 offset1:44
	ds_read2_b32 v[156:157], v143 offset0:48 offset1:52
	ds_read2_b32 v[158:159], v143 offset0:56 offset1:60
	ds_read_b128 v[0:3], v138
	ds_read_b128 v[4:7], v138 offset:1024
	ds_read_b128 v[8:11], v138 offset:2048
	ds_read_b128 v[12:15], v138 offset:3072
	ds_read_b128 v[16:19], v138 offset:4096
	ds_read_b128 v[20:23], v138 offset:5120
	s_waitcnt lgkmcnt(6)
	v_cmp_neq_f32_e64 s[40:41], 0, v144
	v_cmp_neq_f32_e64 s[42:43], 0, v145
	v_cmp_neq_f32_e64 s[44:45], 0, v146
	v_cmp_neq_f32_e64 s[46:47], 0, v147
	v_cmp_neq_f32_e64 s[48:49], 0, v148
	v_cmp_neq_f32_e64 s[50:51], 0, v149
	v_cmp_neq_f32_e64 s[52:53], 0, v150
	v_cmp_neq_f32_e64 s[54:55], 0, v151
	v_cmp_neq_f32_e64 s[56:57], 0, v152
	v_cmp_neq_f32_e64 s[58:59], 0, v153
	v_cmp_neq_f32_e64 s[60:61], 0, v154
	v_cmp_neq_f32_e64 s[62:63], 0, v155
	v_cmp_neq_f32_e64 s[64:65], 0, v156
	v_cmp_neq_f32_e64 s[66:67], 0, v157
	v_cmp_neq_f32_e64 s[68:69], 0, v158
	v_cmp_neq_f32_e64 s[70:71], 0, v159
	s_mov_b64 exec, s[40:41]
	global_load_dwordx4 v[64:67], v138, s[14:15] nt
	s_mov_b64 exec, s[42:43]
	global_load_dwordx4 v[68:71], v138, s[14:15] offset:1024 nt
	s_mov_b64 exec, s[44:45]
	global_load_dwordx4 v[72:75], v138, s[14:15] offset:2048 nt
	s_mov_b64 exec, s[46:47]
	global_load_dwordx4 v[76:79], v138, s[14:15] offset:3072 nt
	s_add_u32 s14, s14, 0x1000
	s_addc_u32 s15, s15, 0
	s_mov_b64 exec, s[48:49]
	global_load_dwordx4 v[80:83], v138, s[14:15] nt
	s_mov_b64 exec, s[50:51]
	global_load_dwordx4 v[84:87], v138, s[14:15] offset:1024 nt
	s_mov_b64 exec, s[52:53]
	global_load_dwordx4 v[88:91], v138, s[14:15] offset:2048 nt
	s_mov_b64 exec, s[54:55]
	global_load_dwordx4 v[92:95], v138, s[14:15] offset:3072 nt
	s_add_u32 s14, s14, 0x1000
	s_addc_u32 s15, s15, 0
	s_mov_b64 exec, s[56:57]
	global_load_dwordx4 v[96:99], v138, s[14:15] nt
	s_mov_b64 exec, s[58:59]
	global_load_dwordx4 v[100:103], v138, s[14:15] offset:1024 nt
	s_mov_b64 exec, s[60:61]
	global_load_dwordx4 v[104:107], v138, s[14:15] offset:2048 nt
	s_mov_b64 exec, s[62:63]
	global_load_dwordx4 v[108:111], v138, s[14:15] offset:3072 nt
	s_add_u32 s14, s14, 0x1000
	s_addc_u32 s15, s15, 0
	s_mov_b64 exec, s[64:65]
	global_load_dwordx4 v[112:115], v138, s[14:15] nt
	s_mov_b64 exec, s[66:67]
	global_load_dwordx4 v[116:119], v138, s[14:15] offset:1024 nt
	s_mov_b64 exec, s[68:69]
	global_load_dwordx4 v[120:123], v138, s[14:15] offset:2048 nt
	s_mov_b64 exec, s[70:71]
	global_load_dwordx4 v[124:127], v138, s[14:15] offset:3072 nt
	s_mov_b64 exec, -1
	v_mov_b32_e32 v160, 0
	v_mov_b32_e32 v161, 0
	v_mov_b32_e32 v162, 0
	v_mov_b32_e32 v163, 0
	v_mov_b32_e32 v164, 0
	v_mov_b32_e32 v165, 0
	v_mov_b32_e32 v166, 0
	v_mov_b32_e32 v167, 0
	s_waitcnt lgkmcnt(0)
	ds_read_b128 v[24:27], v138 offset:6144
	ds_read_b128 v[28:31], v138 offset:7168
	ds_read_b128 v[32:35], v138 offset:8192
	ds_read_b128 v[36:39], v138 offset:9216
	ds_read_b128 v[40:43], v138 offset:10240
	ds_read_b128 v[44:47], v138 offset:11264
	ds_read_b128 v[48:51], v138 offset:12288
	ds_read_b128 v[52:55], v138 offset:13312
	ds_read_b128 v[56:59], v138 offset:14336
	ds_read_b128 v[60:63], v138 offset:15360
	s_waitcnt vmcnt(0)
	s_mov_b64 exec, s[40:41]
	v_pk_fma_f32 v[160:161], v[144:145], v[64:65], v[160:161] op_sel_hi:[0,1,1]
	v_pk_fma_f32 v[162:163], v[144:145], v[66:67], v[162:163] op_sel_hi:[0,1,1]
	s_mov_b64 exec, s[42:43]
	v_pk_fma_f32 v[164:165], v[144:145], v[68:69], v[164:165] op_sel:[1,0,0]
	v_pk_fma_f32 v[166:167], v[144:145], v[70:71], v[166:167] op_sel:[1,0,0]
	s_mov_b64 exec, s[44:45]
	v_pk_fma_f32 v[160:161], v[146:147], v[72:73], v[160:161] op_sel_hi:[0,1,1]
	v_pk_fma_f32 v[162:163], v[146:147], v[74:75], v[162:163] op_sel_hi:[0,1,1]
	s_mov_b64 exec, s[46:47]
	v_pk_fma_f32 v[164:165], v[146:147], v[76:77], v[164:165] op_sel:[1,0,0]
	v_pk_fma_f32 v[166:167], v[146:147], v[78:79], v[166:167] op_sel:[1,0,0]
	s_mov_b64 exec, s[48:49]
	v_pk_fma_f32 v[160:161], v[148:149], v[80:81], v[160:161] op_sel_hi:[0,1,1]
	v_pk_fma_f32 v[162:163], v[148:149], v[82:83], v[162:163] op_sel_hi:[0,1,1]
	s_mov_b64 exec, s[50:51]
	v_pk_fma_f32 v[164:165], v[148:149], v[84:85], v[164:165] op_sel:[1,0,0]
	v_pk_fma_f32 v[166:167], v[148:149], v[86:87], v[166:167] op_sel:[1,0,0]
	s_mov_b64 exec, s[52:53]
	v_pk_fma_f32 v[160:161], v[150:151], v[88:89], v[160:161] op_sel_hi:[0,1,1]
	v_pk_fma_f32 v[162:163], v[150:151], v[90:91], v[162:163] op_sel_hi:[0,1,1]
	s_mov_b64 exec, s[54:55]
	v_pk_fma_f32 v[164:165], v[150:151], v[92:93], v[164:165] op_sel:[1,0,0]
	v_pk_fma_f32 v[166:167], v[150:151], v[94:95], v[166:167] op_sel:[1,0,0]
	s_mov_b64 exec, s[56:57]
	v_pk_fma_f32 v[160:161], v[152:153], v[96:97], v[160:161] op_sel_hi:[0,1,1]
	v_pk_fma_f32 v[162:163], v[152:153], v[98:99], v[162:163] op_sel_hi:[0,1,1]
	s_mov_b64 exec, s[58:59]
	v_pk_fma_f32 v[164:165], v[152:153], v[100:101], v[164:165] op_sel:[1,0,0]
	v_pk_fma_f32 v[166:167], v[152:153], v[102:103], v[166:167] op_sel:[1,0,0]
	s_mov_b64 exec, s[60:61]
	v_pk_fma_f32 v[160:161], v[154:155], v[104:105], v[160:161] op_sel_hi:[0,1,1]
	v_pk_fma_f32 v[162:163], v[154:155], v[106:107], v[162:163] op_sel_hi:[0,1,1]
	s_mov_b64 exec, s[62:63]
	v_pk_fma_f32 v[164:165], v[154:155], v[108:109], v[164:165] op_sel:[1,0,0]
	v_pk_fma_f32 v[166:167], v[154:155], v[110:111], v[166:167] op_sel:[1,0,0]
	s_mov_b64 exec, s[64:65]
	v_pk_fma_f32 v[160:161], v[156:157], v[112:113], v[160:161] op_sel_hi:[0,1,1]
	v_pk_fma_f32 v[162:163], v[156:157], v[114:115], v[162:163] op_sel_hi:[0,1,1]
	s_mov_b64 exec, s[66:67]
	v_pk_fma_f32 v[164:165], v[156:157], v[116:117], v[164:165] op_sel:[1,0,0]
	v_pk_fma_f32 v[166:167], v[156:157], v[118:119], v[166:167] op_sel:[1,0,0]
	s_mov_b64 exec, s[68:69]
	v_pk_fma_f32 v[160:161], v[158:159], v[120:121], v[160:161] op_sel_hi:[0,1,1]
	v_pk_fma_f32 v[162:163], v[158:159], v[122:123], v[162:163] op_sel_hi:[0,1,1]
	s_mov_b64 exec, s[70:71]
	v_pk_fma_f32 v[164:165], v[158:159], v[124:125], v[164:165] op_sel:[1,0,0]
	v_pk_fma_f32 v[166:167], v[158:159], v[126:127], v[166:167] op_sel:[1,0,0]
	s_mov_b64 exec, -1
	v_pk_add_f32 v[160:161], v[160:161], v[164:165]
	v_pk_add_f32 v[162:163], v[162:163], v[166:167]
	s_nop 1
	v_permlane16_swap_b32_e32 v160, v161
	v_permlane16_swap_b32_e32 v162, v163
	v_add_f32_e32 v160, v160, v161
	v_add_f32_e32 v162, v162, v163
	s_nop 1
	v_permlane32_swap_b32_e32 v160, v162
	v_add_f32_e32 v160, v160, v162
	v_add_f32_e32 v160, v160, v137
	s_waitcnt lgkmcnt(0)
	ds_write_b32 v142, v160
	ds_read2_b32 v[144:145], v143 offset0:0 offset1:4
	ds_read2_b32 v[146:147], v143 offset0:8 offset1:12
	ds_read2_b32 v[148:149], v143 offset0:16 offset1:20
	ds_read2_b32 v[150:151], v143 offset0:24 offset1:28
	ds_read2_b32 v[152:153], v143 offset0:32 offset1:36
	ds_read2_b32 v[154:155], v143 offset0:40 offset1:44
	ds_read2_b32 v[156:157], v143 offset0:48 offset1:52
	ds_read2_b32 v[158:159], v143 offset0:56 offset1:60
	v_lshlrev_b32_e32 v136, 3, v140
	v_lshl_or_b32 v136, v139, 2, v136
	v_cmp_gt_u32_e32 vcc, 2, v139
	s_waitcnt lgkmcnt(0)
	v_pk_mul_f32 v[160:161], v[144:145], v[0:1] op_sel_hi:[0,1]
	v_pk_mul_f32 v[162:163], v[144:145], v[2:3] op_sel_hi:[0,1]
	v_pk_mul_f32 v[164:165], v[144:145], v[4:5] op_sel:[1,0]
	v_pk_mul_f32 v[166:167], v[144:145], v[6:7] op_sel:[1,0]
	v_pk_fma_f32 v[160:161], v[146:147], v[8:9], v[160:161] op_sel_hi:[0,1,1]
	v_pk_fma_f32 v[162:163], v[146:147], v[10:11], v[162:163] op_sel_hi:[0,1,1]
	v_pk_fma_f32 v[164:165], v[146:147], v[12:13], v[164:165] op_sel:[1,0,0]
	v_pk_fma_f32 v[166:167], v[146:147], v[14:15], v[166:167] op_sel:[1,0,0]
	v_pk_fma_f32 v[160:161], v[148:149], v[16:17], v[160:161] op_sel_hi:[0,1,1]
	v_pk_fma_f32 v[162:163], v[148:149], v[18:19], v[162:163] op_sel_hi:[0,1,1]
	v_pk_fma_f32 v[164:165], v[148:149], v[20:21], v[164:165] op_sel:[1,0,0]
	v_pk_fma_f32 v[166:167], v[148:149], v[22:23], v[166:167] op_sel:[1,0,0]
	v_pk_fma_f32 v[160:161], v[150:151], v[24:25], v[160:161] op_sel_hi:[0,1,1]
	v_pk_fma_f32 v[162:163], v[150:151], v[26:27], v[162:163] op_sel_hi:[0,1,1]
	v_pk_fma_f32 v[164:165], v[150:151], v[28:29], v[164:165] op_sel:[1,0,0]
	v_pk_fma_f32 v[166:167], v[150:151], v[30:31], v[166:167] op_sel:[1,0,0]
	v_pk_fma_f32 v[160:161], v[152:153], v[32:33], v[160:161] op_sel_hi:[0,1,1]
	v_pk_fma_f32 v[162:163], v[152:153], v[34:35], v[162:163] op_sel_hi:[0,1,1]
	v_pk_fma_f32 v[164:165], v[152:153], v[36:37], v[164:165] op_sel:[1,0,0]
	v_pk_fma_f32 v[166:167], v[152:153], v[38:39], v[166:167] op_sel:[1,0,0]
	v_pk_fma_f32 v[160:161], v[154:155], v[40:41], v[160:161] op_sel_hi:[0,1,1]
	v_pk_fma_f32 v[162:163], v[154:155], v[42:43], v[162:163] op_sel_hi:[0,1,1]
	v_pk_fma_f32 v[164:165], v[154:155], v[44:45], v[164:165] op_sel:[1,0,0]
	v_pk_fma_f32 v[166:167], v[154:155], v[46:47], v[166:167] op_sel:[1,0,0]
	v_pk_fma_f32 v[160:161], v[156:157], v[48:49], v[160:161] op_sel_hi:[0,1,1]
	v_pk_fma_f32 v[162:163], v[156:157], v[50:51], v[162:163] op_sel_hi:[0,1,1]
	v_pk_fma_f32 v[164:165], v[156:157], v[52:53], v[164:165] op_sel:[1,0,0]
	v_pk_fma_f32 v[166:167], v[156:157], v[54:55], v[166:167] op_sel:[1,0,0]
	v_pk_fma_f32 v[160:161], v[158:159], v[56:57], v[160:161] op_sel_hi:[0,1,1]
	v_pk_fma_f32 v[162:163], v[158:159], v[58:59], v[162:163] op_sel_hi:[0,1,1]
	v_pk_fma_f32 v[164:165], v[158:159], v[60:61], v[164:165] op_sel:[1,0,0]
	v_pk_fma_f32 v[166:167], v[158:159], v[62:63], v[166:167] op_sel:[1,0,0]
	v_pk_add_f32 v[160:161], v[160:161], v[164:165]
	v_pk_add_f32 v[162:163], v[162:163], v[166:167]
	s_nop 1
	v_permlane16_swap_b32_e32 v160, v162
	v_permlane16_swap_b32_e32 v161, v163
	v_add_f32_e32 v160, v160, v162
	v_add_f32_e32 v161, v161, v163
	v_mov_b32_e32 v144, v160
	v_mov_b32_e32 v145, v161
	s_nop 1
	v_permlane32_swap_b32_e32 v160, v144
	v_permlane32_swap_b32_e32 v161, v145
	v_add_f32_e32 v160, v160, v144
	v_add_f32_e32 v161, v161, v145
	v_cvt_pk_f16_f32 v137, v160, v161
	s_and_saveexec_b64 s[4:5], vcc
	global_atomic_pk_add_f16 v136, v137, s[20:21]
	s_endpgm
	.p2align	8
